# baseline (speedup 1.0000x reference)
_Z16sum_layer_kernelPKfS0_Pf:
	s_load_dwordx4 s[4:7], s[0:1], 0x0
	s_load_dwordx2 s[8:9], s[0:1], 0x10
	v_lshrrev_b32_e32 v42, 6, v0
	v_bfe_u32 v41, v0, 5, 1
	v_and_b32_e32 v40, 31, v0
	v_readfirstlane_b32 s23, v42
	v_and_b32_e32 v43, 7, v0
	v_bfe_u32 v44, v0, 3, 3
	s_lshr_b32 s40, s23, 1
	s_lshr_b32 s41, s2, 8
	s_xor_b32 s40, s40, s41
	s_and_b32 s40, s40, 1
	s_cmp_eq_u32 s40, 0
	s_cbranch_scc1 .Lno_wave_sleep
	s_sleep 32
.Lno_wave_sleep:
	s_lshl_b32 s3, s2, 12
	s_lshl_b32 s19, s2, 7
	s_lshl_b32 s23, s23, 12
	v_lshlrev_b32_e32 v1, 11, v41
	v_lshl_or_b32 v1, v40, 2, v1
	s_mov_b32 m0, s23
	v_lshrrev_b32_e32 v46, 1, v44
	v_xor_b32_e32 v46, v43, v46
	v_lshlrev_b32_e32 v46, 4, v46
	v_lshl_add_u32 v35, v44, 16, v46
	v_lshl_add_u32 v35, v42, 21, v35
	v_add_u32_e32 v35, s19, v35
	v_xor_b32_e32 v86, 64, v35
	s_mov_b32 s20, 0x7fc00
	s_mov_b32 s21, 0xff800
	s_mov_b32 s22, 0x17f400
	s_mov_b32 s14, 0x200000
	s_mov_b32 s15, 0x20000
	v_and_b32_e32 v45, 63, v0
	v_lshlrev_b32_e32 v37, 4, v45
	s_add_u32 s54, s23, 0x4000
	s_waitcnt lgkmcnt(0)
	s_mov_b32 s12, s6
	s_and_b32 s13, s7, 0xffff
	s_and_b32 s5, s5, 0xffff
	s_mov_b32 s6, 0x800000
	s_mov_b32 s7, s15
	s_mov_b32 m0, s54
	s_nop 0
	buffer_load_dwordx4 v37, s[12:15], s3 offen nt lds
	buffer_load_dwordx4 v37, s[12:15], s3 offen offset:1024 nt lds
	buffer_load_dwordx4 v37, s[12:15], s3 offen offset:2048 nt lds
	buffer_load_dwordx4 v37, s[12:15], s3 offen offset:3072 nt lds
	s_mov_b32 m0, s23
	s_nop 0
	buffer_load_dwordx4 v35, s[4:7], 0 offen nt lds
	buffer_load_dwordx4 v86, s[4:7], s20 offen offset:1024 nt lds
	buffer_load_dwordx4 v35, s[4:7], s21 offen offset:2048 nt lds
	buffer_load_dwordx4 v86, s[4:7], s22 offen offset:3072 nt lds
	v_and_b32_e32 v45, 63, v0
	v_lshlrev_b32_e32 v36, 2, v40
	v_lshl_add_u32 v36, v41, 18, v36
	v_lshl_add_u32 v36, v42, 21, v36
	v_add_u32_e32 v36, s19, v36
	v_bfe_u32 v47, v40, 1, 3
	v_lshlrev_b32_e32 v39, 2, v41
	v_xor_b32_e32 v39, v39, v47
	v_lshlrev_b32_e32 v39, 4, v39
	v_lshl_add_u32 v39, v40, 7, v39
	v_lshl_add_u32 v39, v42, 12, v39
	v_xor_b32_e32 v81, 16, v39
	v_xor_b32_e32 v82, 32, v39
	v_xor_b32_e32 v83, 48, v39
	v_cmp_gt_u32_e32 vcc, 32, v45
	v_mov_b32_e32 v34, 0xc1600000
	v_mov_b32_e32 v84, 0x3fb8aa3b
	v_mov_b32_e32 v85, 0x3f317218
	s_lshl_b32 s24, 1, 16
	s_lshl_b32 s25, 2, 16
	s_lshl_b32 s26, 3, 16
	s_lshl_b32 s27, 8, 16
	s_lshl_b32 s28, 9, 16
	s_lshl_b32 s29, 10, 16
	s_lshl_b32 s30, 11, 16
	s_lshl_b32 s31, 16, 16
	s_lshl_b32 s32, 17, 16
	s_lshl_b32 s33, 18, 16
	s_lshl_b32 s34, 19, 16
	s_lshl_b32 s35, 24, 16
	s_lshl_b32 s36, 25, 16
	s_lshl_b32 s37, 26, 16
	s_lshl_b32 s38, 27, 16
	s_and_b32 s9, s9, 0xffff
	s_mov_b32 s10, s6
	s_mov_b32 s11, s15
	v_lshl_add_u32 v38, v42, 12, v1
	v_add_u32_e32 v38, 0x4000, v38
	v_add_u32_e32 v87, 0x400, v38
	s_waitcnt vmcnt(4)
	ds_read2_b32 v[18:19], v38 offset0:0 offset1:32
	ds_read2_b32 v[20:21], v38 offset0:64 offset1:96
	ds_read2_b32 v[22:23], v38 offset0:128 offset1:160
	ds_read2_b32 v[24:25], v38 offset0:192 offset1:224
	ds_read2_b32 v[26:27], v87 offset0:0 offset1:32
	ds_read2_b32 v[28:29], v87 offset0:64 offset1:96
	ds_read2_b32 v[30:31], v87 offset0:128 offset1:160
	ds_read2_b32 v[32:33], v87 offset0:192 offset1:224
	s_waitcnt lgkmcnt(0)
	v_max3_f32 v48, v18, v19, v20
	v_max3_f32 v50, v21, v22, v23
	v_max3_f32 v48, v48, v24, v25
	v_max3_f32 v50, v50, v26, v27
	v_max3_f32 v48, v48, v28, v29
	v_max3_f32 v50, v50, v30, v31
	v_max3_f32 v48, v48, v32, v33
	v_max_f32_e32 v48, v48, v50
	v_mov_b32_e32 v50, v48
	s_nop 1
	v_permlane32_swap_b32_e32 v48, v50
	v_max_f32_e32 v48, v48, v50
	v_fmamk_f32 v48, v48, 0x3fb8aa3b, v34
	v_pk_fma_f32 v[18:19], v[18:19], v[84:85], v[48:49] op_sel_hi:[1,0,0] neg_lo:[0,0,1] neg_hi:[0,0,1]
	v_exp_f32_e32 v18, v18
	v_exp_f32_e32 v19, v19
	v_pk_fma_f32 v[20:21], v[20:21], v[84:85], v[48:49] op_sel_hi:[1,0,0] neg_lo:[0,0,1] neg_hi:[0,0,1]
	v_exp_f32_e32 v20, v20
	v_exp_f32_e32 v21, v21
	v_pk_fma_f32 v[22:23], v[22:23], v[84:85], v[48:49] op_sel_hi:[1,0,0] neg_lo:[0,0,1] neg_hi:[0,0,1]
	v_exp_f32_e32 v22, v22
	v_exp_f32_e32 v23, v23
	v_pk_fma_f32 v[24:25], v[24:25], v[84:85], v[48:49] op_sel_hi:[1,0,0] neg_lo:[0,0,1] neg_hi:[0,0,1]
	v_exp_f32_e32 v24, v24
	v_exp_f32_e32 v25, v25
	v_pk_fma_f32 v[26:27], v[26:27], v[84:85], v[48:49] op_sel_hi:[1,0,0] neg_lo:[0,0,1] neg_hi:[0,0,1]
	v_exp_f32_e32 v26, v26
	v_exp_f32_e32 v27, v27
	v_pk_fma_f32 v[28:29], v[28:29], v[84:85], v[48:49] op_sel_hi:[1,0,0] neg_lo:[0,0,1] neg_hi:[0,0,1]
	v_exp_f32_e32 v28, v28
	v_exp_f32_e32 v29, v29
	v_pk_fma_f32 v[30:31], v[30:31], v[84:85], v[48:49] op_sel_hi:[1,0,0] neg_lo:[0,0,1] neg_hi:[0,0,1]
	v_exp_f32_e32 v30, v30
	v_exp_f32_e32 v31, v31
	v_pk_fma_f32 v[32:33], v[32:33], v[84:85], v[48:49] op_sel_hi:[1,0,0] neg_lo:[0,0,1] neg_hi:[0,0,1]
	v_exp_f32_e32 v32, v32
	v_exp_f32_e32 v33, v33
	v_pk_add_f32 v[56:57], v[18:19], v[20:21]
	v_pk_add_f32 v[58:59], v[22:23], v[24:25]
	v_pk_add_f32 v[60:61], v[26:27], v[28:29]
	v_pk_add_f32 v[62:63], v[30:31], v[32:33]
	v_pk_add_f32 v[56:57], v[56:57], v[58:59]
	v_pk_add_f32 v[60:61], v[60:61], v[62:63]
	v_pk_add_f32 v[56:57], v[56:57], v[60:61]
	v_add_f32_e32 v50, v56, v57
	v_mov_b32_e32 v51, v50
	s_nop 1
	v_permlane32_swap_b32_e32 v50, v51
	v_add_f32_e32 v50, v50, v51
	v_log_f32_e32 v50, v50
	v_cvt_pk_f16_f32 v40, v18, v19
	v_cvt_pk_f16_f32 v41, v20, v21
	v_cvt_pk_f16_f32 v42, v22, v23
	v_cvt_pk_f16_f32 v43, v24, v25
	v_cvt_pk_f16_f32 v44, v26, v27
	v_cvt_pk_f16_f32 v45, v28, v29
	v_cvt_pk_f16_f32 v46, v30, v31
	v_cvt_pk_f16_f32 v47, v32, v33
	v_add_f32_e32 v50, 0x41600000, v50
	v_mul_f32_e32 v50, 0xbf317218, v50
	v_cndmask_b32_e64 v51, v50, 1.0, vcc
	s_waitcnt vmcnt(0)
	ds_read_b128 v[2:5], v39
	ds_read_b128 v[6:9], v81
	ds_read_b128 v[10:13], v82
	ds_read_b128 v[14:17], v83
	s_waitcnt lgkmcnt(2)
	v_max3_f32 v52, v2, v3, v4
	v_max3_f32 v53, v5, v6, v7
	v_max_f32_e32 v52, v52, v8
	v_max_f32_e32 v53, v53, v9
	s_waitcnt lgkmcnt(0)
	v_max3_f32 v52, v52, v10, v11
	v_max3_f32 v53, v53, v12, v13
	v_max3_f32 v52, v52, v14, v15
	v_max3_f32 v53, v53, v16, v17
	v_max_f32_e32 v52, v52, v53
	v_mov_b32_e32 v53, v52
	s_nop 1
	v_permlane32_swap_b32_e32 v52, v53
	v_max_f32_e32 v52, v52, v53
	v_cndmask_b32_e32 v54, 1.0, v52, vcc
	v_fmamk_f32 v48, v52, 0x3fb8aa3b, v34
	v_pk_fma_f32 v[2:3], v[2:3], v[84:85], v[48:49] op_sel_hi:[1,0,0] neg_lo:[0,0,1] neg_hi:[0,0,1]
	v_mfma_f32_32x32x2_f32 v[64:79], v54, v51, 0
	v_exp_f32_e32 v2, v2
	v_exp_f32_e32 v3, v3
	v_pk_fma_f32 v[4:5], v[4:5], v[84:85], v[48:49] op_sel_hi:[1,0,0] neg_lo:[0,0,1] neg_hi:[0,0,1]
	v_exp_f32_e32 v4, v4
	v_exp_f32_e32 v5, v5
	v_pk_fma_f32 v[6:7], v[6:7], v[84:85], v[48:49] op_sel_hi:[1,0,0] neg_lo:[0,0,1] neg_hi:[0,0,1]
	v_exp_f32_e32 v6, v6
	v_exp_f32_e32 v7, v7
	v_pk_fma_f32 v[8:9], v[8:9], v[84:85], v[48:49] op_sel_hi:[1,0,0] neg_lo:[0,0,1] neg_hi:[0,0,1]
	v_exp_f32_e32 v8, v8
	v_exp_f32_e32 v9, v9
	v_pk_fma_f32 v[10:11], v[10:11], v[84:85], v[48:49] op_sel_hi:[1,0,0] neg_lo:[0,0,1] neg_hi:[0,0,1]
	v_exp_f32_e32 v10, v10
	v_cvt_pk_f16_f32 v56, v2, v3
	v_cvt_pk_f16_f32 v57, v4, v5
	v_cvt_pk_f16_f32 v58, v6, v7
	v_cvt_pk_f16_f32 v59, v8, v9
	v_exp_f32_e32 v11, v11
	v_pk_fma_f32 v[12:13], v[12:13], v[84:85], v[48:49] op_sel_hi:[1,0,0] neg_lo:[0,0,1] neg_hi:[0,0,1]
	v_exp_f32_e32 v12, v12
	v_mfma_f32_32x32x16_f16 v[18:33], v[56:59], v[40:43], 0
	v_exp_f32_e32 v13, v13
	v_pk_fma_f32 v[14:15], v[14:15], v[84:85], v[48:49] op_sel_hi:[1,0,0] neg_lo:[0,0,1] neg_hi:[0,0,1]
	v_exp_f32_e32 v14, v14
	v_exp_f32_e32 v15, v15
	v_pk_fma_f32 v[16:17], v[16:17], v[84:85], v[48:49] op_sel_hi:[1,0,0] neg_lo:[0,0,1] neg_hi:[0,0,1]
	v_exp_f32_e32 v16, v16
	v_exp_f32_e32 v17, v17
	v_cvt_pk_f16_f32 v60, v10, v11
	v_cvt_pk_f16_f32 v61, v12, v13
	v_cvt_pk_f16_f32 v62, v14, v15
	v_cvt_pk_f16_f32 v63, v16, v17
	s_nop 1
	v_mfma_f32_32x32x16_f16 v[18:33], v[60:63], v[44:47], v[18:33]
	s_nop 11
	v_log_f32_e32 v18, v18
	v_log_f32_e32 v19, v19
	v_log_f32_e32 v20, v20
	v_log_f32_e32 v21, v21
	v_log_f32_e32 v22, v22
	v_log_f32_e32 v23, v23
	v_pk_fma_f32 v[64:65], v[18:19], v[84:85], v[64:65] op_sel:[0,1,0] op_sel_hi:[1,1,1]
	buffer_store_dword v64, v36, s[8:11], 0 offen
	buffer_store_dword v65, v36, s[8:11], s24 offen
	v_log_f32_e32 v24, v24
	v_log_f32_e32 v25, v25
	v_pk_fma_f32 v[66:67], v[20:21], v[84:85], v[66:67] op_sel:[0,1,0] op_sel_hi:[1,1,1]
	buffer_store_dword v66, v36, s[8:11], s25 offen
	buffer_store_dword v67, v36, s[8:11], s26 offen
	v_log_f32_e32 v26, v26
	v_log_f32_e32 v27, v27
	v_pk_fma_f32 v[68:69], v[22:23], v[84:85], v[68:69] op_sel:[0,1,0] op_sel_hi:[1,1,1]
	buffer_store_dword v68, v36, s[8:11], s27 offen
	buffer_store_dword v69, v36, s[8:11], s28 offen
	v_log_f32_e32 v28, v28
	v_log_f32_e32 v29, v29
	v_pk_fma_f32 v[70:71], v[24:25], v[84:85], v[70:71] op_sel:[0,1,0] op_sel_hi:[1,1,1]
	buffer_store_dword v70, v36, s[8:11], s29 offen
	buffer_store_dword v71, v36, s[8:11], s30 offen
	v_log_f32_e32 v30, v30
	v_log_f32_e32 v31, v31
	v_pk_fma_f32 v[72:73], v[26:27], v[84:85], v[72:73] op_sel:[0,1,0] op_sel_hi:[1,1,1]
	buffer_store_dword v72, v36, s[8:11], s31 offen
	buffer_store_dword v73, v36, s[8:11], s32 offen
	v_log_f32_e32 v32, v32
	v_log_f32_e32 v33, v33
	v_pk_fma_f32 v[74:75], v[28:29], v[84:85], v[74:75] op_sel:[0,1,0] op_sel_hi:[1,1,1]
	buffer_store_dword v74, v36, s[8:11], s33 offen
	buffer_store_dword v75, v36, s[8:11], s34 offen
	v_pk_fma_f32 v[76:77], v[30:31], v[84:85], v[76:77] op_sel:[0,1,0] op_sel_hi:[1,1,1]
	buffer_store_dword v76, v36, s[8:11], s35 offen
	buffer_store_dword v77, v36, s[8:11], s36 offen
	v_pk_fma_f32 v[78:79], v[32:33], v[84:85], v[78:79] op_sel:[0,1,0] op_sel_hi:[1,1,1]
	buffer_store_dword v78, v36, s[8:11], s37 offen
	buffer_store_dword v79, v36, s[8:11], s38 offen
	s_endpgm
